# grid-barrier poll loops of the layer loop without s_sleep between polls (tighter release detection), on the v80 build
# speedup vs baseline: 1.0015x; 1.0014x over previous
; __device__ __forceinline__ unsigned xb_ld(unsigned* p)              { return __hip_atomic_load(p, __ATOMIC_RELAXED, __HIP_MEMORY_SCOPE_AGENT); }
; __device__ __forceinline__ void xcd_barrier_complete(unsigned* bar, unsigned x, unsigned& nloc, unsigned& nx) {
;     ...
;     for (;;) {
;         sum = 0u; cnt = 0u; mine = 0u;
; #pragma unroll
;         for (unsigned j = 0; j < 16; ++j) { const unsigned c = xb_ld(&bar[XB_XCNT(j)]); sum += c; cnt += (c > 0u) ? 1u : 0u; mine = (j == x) ? c : mine; }
;         if (sum == G) break;
;         __builtin_amdgcn_s_sleep(1);
;         if ((++sp & 255u) == 0u) { if (xb_ld(&bar[XB_TMO])) break; if (sp > XB_SPIN_CAP) { atomicAdd(&bar[XB_TMO], 1u); break; } }
;     }
.LBB0_232:
	global_load_dword v16, v1, s[10:11] sc1
	global_load_dword v0, v1, s[12:13] sc1
	global_load_dword v2, v1, s[14:15] sc1
	global_load_dword v3, v1, s[16:17] sc1
	global_load_dword v4, v1, s[18:19] sc1
	global_load_dword v5, v1, s[20:21] sc1
	global_load_dword v6, v1, s[22:23] sc1
	global_load_dword v7, v1, s[24:25] sc1
	global_load_dword v8, v1, s[26:27] sc1
	global_load_dword v9, v1, s[28:29] sc1
	global_load_dword v10, v1, s[30:31] sc1
	global_load_dword v11, v1, s[34:35] sc1
	global_load_dword v12, v1, s[36:37] sc1
	global_load_dword v13, v1, s[38:39] sc1
	global_load_dword v14, v1, s[40:41] sc1
	global_load_dword v15, v1, s[44:45] sc1
	s_mov_b64 s[46:47], -1
	s_mov_b64 s[48:49], -1
	s_waitcnt vmcnt(14)
	v_add_u32_e32 v17, v0, v16
	s_waitcnt vmcnt(13)
	v_add_u32_e32 v17, v17, v2
	s_waitcnt vmcnt(12)
	v_add_u32_e32 v17, v17, v3
	s_waitcnt vmcnt(11)
	v_add_u32_e32 v17, v17, v4
	s_waitcnt vmcnt(10)
	v_add_u32_e32 v17, v17, v5
	s_waitcnt vmcnt(9)
	v_add_u32_e32 v17, v17, v6
	s_waitcnt vmcnt(8)
	v_add_u32_e32 v17, v17, v7
	s_waitcnt vmcnt(7)
	v_add_u32_e32 v17, v17, v8
	s_waitcnt vmcnt(6)
	v_add_u32_e32 v17, v17, v9
	s_waitcnt vmcnt(5)
	v_add_u32_e32 v17, v17, v10
	s_waitcnt vmcnt(4)
	v_add_u32_e32 v17, v17, v11
	s_waitcnt vmcnt(3)
	v_add_u32_e32 v17, v17, v12
	s_waitcnt vmcnt(2)
	v_add_u32_e32 v17, v17, v13
	s_waitcnt vmcnt(1)
	v_add_u32_e32 v17, v17, v14
	s_waitcnt vmcnt(0)
	v_add_u32_e32 v17, v17, v15
	v_cmp_eq_u32_e32 vcc, s1, v17
	s_cbranch_vccnz .LBB0_231
	s_and_b32 s3, s2, 0xff
	s_cmp_eq_u32 s3, 0
	s_mov_b64 s[50:51], -1
	s_nop 0
	s_cbranch_scc1 .LBB0_236
	s_and_b64 vcc, exec, s[50:51]
	s_cbranch_vccz .LBB0_231

.LBB0_250:
	s_and_b32 s1, s0, 0xff
	s_mov_b64 s[20:21], -1
	s_cmp_lg_u32 s1, 0
	s_mov_b64 s[24:25], -1
	s_nop 0
	s_cbranch_scc0 .LBB0_253
	s_and_b64 vcc, exec, s[24:25]
	s_cbranch_vccz .LBB0_249

.LBB0_267:
	s_and_b32 s1, s0, 0xff
	s_mov_b64 s[16:17], -1
	s_cmp_lg_u32 s1, 0
	s_mov_b64 s[20:21], -1
	s_nop 0
	s_cbranch_scc0 .LBB0_270
	s_and_b64 vcc, exec, s[20:21]
	s_cbranch_vccz .LBB0_266

; __device__ __forceinline__ unsigned xb_ld(unsigned* p)              { return __hip_atomic_load(p, __ATOMIC_RELAXED, __HIP_MEMORY_SCOPE_AGENT); }
; __device__ __forceinline__ void xcd_barrier_complete(unsigned* bar, unsigned x, unsigned& nloc, unsigned& nx) {
;     ...
;     for (;;) {
;         sum = 0u; cnt = 0u; mine = 0u;
; #pragma unroll
;         for (unsigned j = 0; j < 16; ++j) { const unsigned c = xb_ld(&bar[XB_XCNT(j)]); sum += c; cnt += (c > 0u) ? 1u : 0u; mine = (j == x) ? c : mine; }
;         if (sum == G) break;
;         __builtin_amdgcn_s_sleep(1);
;         if ((++sp & 255u) == 0u) { if (xb_ld(&bar[XB_TMO])) break; if (sp > XB_SPIN_CAP) { atomicAdd(&bar[XB_TMO], 1u); break; } }
;     }
.LBB0_379:
	global_load_dword v16, v1, s[10:11] sc1
	global_load_dword v0, v1, s[12:13] sc1
	global_load_dword v2, v1, s[14:15] sc1
	global_load_dword v3, v1, s[16:17] sc1
	global_load_dword v4, v1, s[18:19] sc1
	global_load_dword v5, v1, s[20:21] sc1
	global_load_dword v6, v1, s[22:23] sc1
	global_load_dword v7, v1, s[24:25] sc1
	global_load_dword v8, v1, s[26:27] sc1
	global_load_dword v9, v1, s[28:29] sc1
	global_load_dword v10, v1, s[30:31] sc1
	global_load_dword v11, v1, s[34:35] sc1
	global_load_dword v12, v1, s[36:37] sc1
	global_load_dword v13, v1, s[38:39] sc1
	global_load_dword v14, v1, s[40:41] sc1
	global_load_dword v15, v1, s[42:43] sc1
	s_mov_b64 s[44:45], -1
	s_mov_b64 s[46:47], -1
	s_waitcnt vmcnt(14)
	v_add_u32_e32 v17, v0, v16
	s_waitcnt vmcnt(13)
	v_add_u32_e32 v17, v17, v2
	s_waitcnt vmcnt(12)
	v_add_u32_e32 v17, v17, v3
	s_waitcnt vmcnt(11)
	v_add_u32_e32 v17, v17, v4
	s_waitcnt vmcnt(10)
	v_add_u32_e32 v17, v17, v5
	s_waitcnt vmcnt(9)
	v_add_u32_e32 v17, v17, v6
	s_waitcnt vmcnt(8)
	v_add_u32_e32 v17, v17, v7
	s_waitcnt vmcnt(7)
	v_add_u32_e32 v17, v17, v8
	s_waitcnt vmcnt(6)
	v_add_u32_e32 v17, v17, v9
	s_waitcnt vmcnt(5)
	v_add_u32_e32 v17, v17, v10
	s_waitcnt vmcnt(4)
	v_add_u32_e32 v17, v17, v11
	s_waitcnt vmcnt(3)
	v_add_u32_e32 v17, v17, v12
	s_waitcnt vmcnt(2)
	v_add_u32_e32 v17, v17, v13
	s_waitcnt vmcnt(1)
	v_add_u32_e32 v17, v17, v14
	s_waitcnt vmcnt(0)
	v_add_u32_e32 v17, v17, v15
	v_cmp_eq_u32_e32 vcc, s1, v17
	s_cbranch_vccnz .LBB0_378
	s_and_b32 s3, s2, 0xff
	s_cmp_eq_u32 s3, 0
	s_mov_b64 s[48:49], -1
	s_nop 0
	s_cbranch_scc1 .LBB0_383
	s_and_b64 vcc, exec, s[48:49]
	s_cbranch_vccz .LBB0_378

; __device__ __forceinline__ unsigned xb_ld(unsigned* p)              { return __hip_atomic_load(p, __ATOMIC_RELAXED, __HIP_MEMORY_SCOPE_AGENT); }
; __device__ __forceinline__ void xcd_barrier_complete(unsigned* bar, unsigned x, unsigned& nloc, unsigned& nx) {
;     ...
;     for (;;) {
;         sum = 0u; cnt = 0u; mine = 0u;
; #pragma unroll
;         for (unsigned j = 0; j < 16; ++j) { const unsigned c = xb_ld(&bar[XB_XCNT(j)]); sum += c; cnt += (c > 0u) ? 1u : 0u; mine = (j == x) ? c : mine; }
;         if (sum == G) break;
;         __builtin_amdgcn_s_sleep(1);
;         if ((++sp & 255u) == 0u) { if (xb_ld(&bar[XB_TMO])) break; if (sp > XB_SPIN_CAP) { atomicAdd(&bar[XB_TMO], 1u); break; } }
;     }
.LBB0_647:
	global_load_dword v16, v1, s[10:11] sc1
	global_load_dword v0, v1, s[12:13] sc1
	global_load_dword v2, v1, s[14:15] sc1
	global_load_dword v3, v1, s[16:17] sc1
	global_load_dword v4, v1, s[18:19] sc1
	global_load_dword v5, v1, s[20:21] sc1
	global_load_dword v6, v1, s[24:25] sc1
	global_load_dword v7, v1, s[26:27] sc1
	global_load_dword v8, v1, s[28:29] sc1
	global_load_dword v9, v1, s[30:31] sc1
	global_load_dword v10, v1, s[34:35] sc1
	global_load_dword v11, v1, s[36:37] sc1
	global_load_dword v12, v1, s[38:39] sc1
	global_load_dword v13, v1, s[40:41] sc1
	global_load_dword v14, v1, s[42:43] sc1
	global_load_dword v15, v1, s[44:45] sc1
	s_mov_b64 s[46:47], -1
	s_mov_b64 s[48:49], -1
	s_waitcnt vmcnt(14)
	v_add_u32_e32 v17, v0, v16
	s_waitcnt vmcnt(13)
	v_add_u32_e32 v17, v17, v2
	s_waitcnt vmcnt(12)
	v_add_u32_e32 v17, v17, v3
	s_waitcnt vmcnt(11)
	v_add_u32_e32 v17, v17, v4
	s_waitcnt vmcnt(10)
	v_add_u32_e32 v17, v17, v5
	s_waitcnt vmcnt(9)
	v_add_u32_e32 v17, v17, v6
	s_waitcnt vmcnt(8)
	v_add_u32_e32 v17, v17, v7
	s_waitcnt vmcnt(7)
	v_add_u32_e32 v17, v17, v8
	s_waitcnt vmcnt(6)
	v_add_u32_e32 v17, v17, v9
	s_waitcnt vmcnt(5)
	v_add_u32_e32 v17, v17, v10
	s_waitcnt vmcnt(4)
	v_add_u32_e32 v17, v17, v11
	s_waitcnt vmcnt(3)
	v_add_u32_e32 v17, v17, v12
	s_waitcnt vmcnt(2)
	v_add_u32_e32 v17, v17, v13
	s_waitcnt vmcnt(1)
	v_add_u32_e32 v17, v17, v14
	s_waitcnt vmcnt(0)
	v_add_u32_e32 v17, v17, v15
	v_cmp_eq_u32_e32 vcc, s1, v17
	s_cbranch_vccnz .LBB0_646
	s_and_b32 s3, s2, 0xff
	s_cmp_eq_u32 s3, 0
	s_mov_b64 s[50:51], -1
	s_nop 0
	s_cbranch_scc1 .LBB0_651
	s_and_b64 vcc, exec, s[50:51]
	s_cbranch_vccz .LBB0_646

.LBB0_665:
	s_and_b32 s1, s0, 0xff
	s_mov_b64 s[20:21], -1
	s_cmp_lg_u32 s1, 0
	s_mov_b64 s[26:27], -1
	s_nop 0
	s_cbranch_scc0 .LBB0_668
	s_and_b64 vcc, exec, s[26:27]
	s_cbranch_vccz .LBB0_664

; __device__ __forceinline__ unsigned xb_ld(unsigned* p)              { return __hip_atomic_load(p, __ATOMIC_RELAXED, __HIP_MEMORY_SCOPE_AGENT); }
; __device__ __forceinline__ void xcd_barrier_complete(unsigned* bar, unsigned x, unsigned& nloc, unsigned& nx) {
;     ...
;     for (;;) {
;         sum = 0u; cnt = 0u; mine = 0u;
; #pragma unroll
;         for (unsigned j = 0; j < 16; ++j) { const unsigned c = xb_ld(&bar[XB_XCNT(j)]); sum += c; cnt += (c > 0u) ? 1u : 0u; mine = (j == x) ? c : mine; }
;         if (sum == G) break;
;         __builtin_amdgcn_s_sleep(1);
;         if ((++sp & 255u) == 0u) { if (xb_ld(&bar[XB_TMO])) break; if (sp > XB_SPIN_CAP) { atomicAdd(&bar[XB_TMO], 1u); break; } }
;     }
.LBB0_2015:
	global_load_dword v16, v1, s[12:13] sc1
	global_load_dword v0, v1, s[14:15] sc1
	global_load_dword v2, v1, s[16:17] sc1
	global_load_dword v3, v1, s[18:19] sc1
	global_load_dword v4, v1, s[20:21] sc1
	global_load_dword v5, v1, s[22:23] sc1
	global_load_dword v6, v1, s[24:25] sc1
	global_load_dword v7, v1, s[26:27] sc1
	global_load_dword v8, v1, s[28:29] sc1
	global_load_dword v9, v1, s[30:31] sc1
	global_load_dword v10, v1, s[34:35] sc1
	global_load_dword v11, v1, s[36:37] sc1
	global_load_dword v12, v1, s[38:39] sc1
	global_load_dword v13, v1, s[40:41] sc1
	global_load_dword v14, v1, s[42:43] sc1
	global_load_dword v15, v1, s[44:45] sc1
	s_mov_b64 s[46:47], -1
	s_mov_b64 s[48:49], -1
	s_waitcnt vmcnt(14)
	v_add_u32_e32 v17, v0, v16
	s_waitcnt vmcnt(13)
	v_add_u32_e32 v17, v17, v2
	s_waitcnt vmcnt(12)
	v_add_u32_e32 v17, v17, v3
	s_waitcnt vmcnt(11)
	v_add_u32_e32 v17, v17, v4
	s_waitcnt vmcnt(10)
	v_add_u32_e32 v17, v17, v5
	s_waitcnt vmcnt(9)
	v_add_u32_e32 v17, v17, v6
	s_waitcnt vmcnt(8)
	v_add_u32_e32 v17, v17, v7
	s_waitcnt vmcnt(7)
	v_add_u32_e32 v17, v17, v8
	s_waitcnt vmcnt(6)
	v_add_u32_e32 v17, v17, v9
	s_waitcnt vmcnt(5)
	v_add_u32_e32 v17, v17, v10
	s_waitcnt vmcnt(4)
	v_add_u32_e32 v17, v17, v11
	s_waitcnt vmcnt(3)
	v_add_u32_e32 v17, v17, v12
	s_waitcnt vmcnt(2)
	v_add_u32_e32 v17, v17, v13
	s_waitcnt vmcnt(1)
	v_add_u32_e32 v17, v17, v14
	s_waitcnt vmcnt(0)
	v_add_u32_e32 v17, v17, v15
	v_cmp_eq_u32_e32 vcc, s1, v17
	s_cbranch_vccnz .LBB0_2014
	s_and_b32 s3, s2, 0xff
	s_cmp_eq_u32 s3, 0
	s_mov_b64 s[50:51], -1
	s_nop 0
	s_cbranch_scc1 .LBB0_2019
	s_and_b64 vcc, exec, s[50:51]
	s_cbranch_vccz .LBB0_2014

.LBB0_2033:
	s_and_b32 s1, s0, 0xff
	s_mov_b64 s[22:23], -1
	s_cmp_lg_u32 s1, 0
	s_mov_b64 s[26:27], -1
	s_nop 0
	s_cbranch_scc0 .LBB0_2036
	s_and_b64 vcc, exec, s[26:27]
	s_cbranch_vccz .LBB0_2032

.LBB0_2050:
	s_and_b32 s1, s0, 0xff
	s_mov_b64 s[18:19], -1
	s_cmp_lg_u32 s1, 0
	s_mov_b64 s[22:23], -1
	s_nop 0
	s_cbranch_scc0 .LBB0_2053
	s_and_b64 vcc, exec, s[22:23]
	s_cbranch_vccz .LBB0_2049

; __device__ __forceinline__ unsigned xb_ld(unsigned* p)              { return __hip_atomic_load(p, __ATOMIC_RELAXED, __HIP_MEMORY_SCOPE_AGENT); }
; __device__ __forceinline__ void xcd_barrier_complete(unsigned* bar, unsigned x, unsigned& nloc, unsigned& nx) {
;     ...
;     for (;;) {
;         sum = 0u; cnt = 0u; mine = 0u;
; #pragma unroll
;         for (unsigned j = 0; j < 16; ++j) { const unsigned c = xb_ld(&bar[XB_XCNT(j)]); sum += c; cnt += (c > 0u) ? 1u : 0u; mine = (j == x) ? c : mine; }
;         if (sum == G) break;
;         __builtin_amdgcn_s_sleep(1);
;         if ((++sp & 255u) == 0u) { if (xb_ld(&bar[XB_TMO])) break; if (sp > XB_SPIN_CAP) { atomicAdd(&bar[XB_TMO], 1u); break; } }
;     }
.LBB0_2288:
	global_load_dword v16, v1, s[10:11] sc1
	global_load_dword v0, v1, s[12:13] sc1
	global_load_dword v2, v1, s[16:17] sc1
	global_load_dword v3, v1, s[18:19] sc1
	global_load_dword v4, v1, s[20:21] sc1
	global_load_dword v5, v1, s[22:23] sc1
	global_load_dword v6, v1, s[24:25] sc1
	global_load_dword v7, v1, s[26:27] sc1
	global_load_dword v8, v1, s[28:29] sc1
	global_load_dword v9, v1, s[30:31] sc1
	global_load_dword v10, v1, s[34:35] sc1
	global_load_dword v11, v1, s[36:37] sc1
	global_load_dword v12, v1, s[38:39] sc1
	global_load_dword v13, v1, s[40:41] sc1
	global_load_dword v14, v1, s[42:43] sc1
	global_load_dword v15, v1, s[44:45] sc1
	s_mov_b64 s[46:47], -1
	s_mov_b64 s[48:49], -1
	s_waitcnt vmcnt(14)
	v_add_u32_e32 v17, v0, v16
	s_waitcnt vmcnt(13)
	v_add_u32_e32 v17, v17, v2
	s_waitcnt vmcnt(12)
	v_add_u32_e32 v17, v17, v3
	s_waitcnt vmcnt(11)
	v_add_u32_e32 v17, v17, v4
	s_waitcnt vmcnt(10)
	v_add_u32_e32 v17, v17, v5
	s_waitcnt vmcnt(9)
	v_add_u32_e32 v17, v17, v6
	s_waitcnt vmcnt(8)
	v_add_u32_e32 v17, v17, v7
	s_waitcnt vmcnt(7)
	v_add_u32_e32 v17, v17, v8
	s_waitcnt vmcnt(6)
	v_add_u32_e32 v17, v17, v9
	s_waitcnt vmcnt(5)
	v_add_u32_e32 v17, v17, v10
	s_waitcnt vmcnt(4)
	v_add_u32_e32 v17, v17, v11
	s_waitcnt vmcnt(3)
	v_add_u32_e32 v17, v17, v12
	s_waitcnt vmcnt(2)
	v_add_u32_e32 v17, v17, v13
	s_waitcnt vmcnt(1)
	v_add_u32_e32 v17, v17, v14
	s_waitcnt vmcnt(0)
	v_add_u32_e32 v17, v17, v15
	v_cmp_eq_u32_e32 vcc, s1, v17
	s_cbranch_vccnz .LBB0_2287
	s_and_b32 s3, s2, 0xff
	s_cmp_eq_u32 s3, 0
	s_mov_b64 s[50:51], -1
	s_nop 0
	s_cbranch_scc1 .LBB0_2292
	s_and_b64 vcc, exec, s[50:51]
	s_cbranch_vccz .LBB0_2287
